# NSA block selection: binary-search step tests the ballot count with s_cmp on the scalar count instead of a VALU 64-bit compare + s_and (shorter serial chain); on top of v-permlane NSA exchanges + rout
# baseline (speedup 1.0000x reference)
; __device__ __forceinline__ void nsa_mfma_phase(Frame& F, int l, bf16* YC, int ypitch) {
;     ...
;         for (int i = 0; i < 8; ++i) { int tq = 8 * w + i; asm volatile("" : "+s"(tq)); int ls = lane; asm volatile("" : "+v"(ls)); const float v = (IMP[(0 * 64 + tq) * 65 + ls] + IMP[(1 * 64 + tq) * 65 + ls]) + (IMP[(2 * 64 + tq) * 65 + ls] + IMP[(3 * 64 + tq) * 65 + ls]);
;             const unsigned key = (lane == 0 || lane == c) ? 0xFFFFFFFFu : (lane <= c ? __builtin_bit_cast(unsigned, v) + 1u : 0u);
;             unsigned cur = 0u;
; #pragma unroll
;     ...
;             const unsigned long long gt_ = __ballot(key > cur); unsigned long long eq_ = __ballot(key == cur); const int need = TOPN - __builtin_popcountll(gt_);
;             unsigned long long pick = 0ull;
;             for (int k = 0; k < need; ++k) { const unsigned long long b1 = eq_ & (0ull - eq_); pick |= b1; eq_ ^= b1; }
.LBB0_504:
	s_or_b32 s8, s5, s48
	v_mov_b32_e32 v0, v123
	s_mul_i32 s0, s8, 0x104
	s_add_i32 s0, s0, 0
	s_add_i32 s1, s0, 0xc000
	v_lshlrev_b32_e32 v0, 2, v0
	v_add_u32_e32 v36, s0, v0
	v_add_u32_e32 v0, s1, v0
	ds_read2st64_b32 v[34:35], v0 offset0:65 offset1:130
	ds_read_b32 v0, v0 offset:49920
	ds_read_b32 v36, v36 offset:49152
	s_waitcnt lgkmcnt(2)
	v_mov_b32_e32 v37, v35
	s_waitcnt lgkmcnt(1)
	v_mov_b32_e32 v35, v0
	s_waitcnt lgkmcnt(0)
	v_pk_add_f32 v[34:35], v[36:37], v[34:35]
	s_nop 0
	v_pk_add_f32 v[34:35], v[34:35], v[34:35] op_sel:[0,1] op_sel_hi:[1,0]
	s_nop 0
	v_add_u32_e32 v0, 1, v34
	v_cndmask_b32_e64 v0, v0, 0, s[44:45]
	v_cndmask_b32_e64 v0, v0, -1, s[2:3]
	v_cmp_gt_i32_e32 vcc, 0, v0
	s_bcnt1_i32_b64 s88, vcc
	s_cmp_gt_u32 s88, 15
	s_cselect_b32 s9, 0x80000000, 0
	s_or_b32 s10, s9, 2.0
	v_cmp_le_u32_e32 vcc, s10, v0
	s_bcnt1_i32_b64 s88, vcc
	s_cmp_gt_u32 s88, 15
	s_cselect_b32 s9, s10, s9
	s_or_b32 s10, s9, 0x20000000
	v_cmp_le_u32_e32 vcc, s10, v0
	s_bcnt1_i32_b64 s88, vcc
	s_cmp_gt_u32 s88, 15
	s_cselect_b32 s9, s10, s9
	s_or_b32 s10, s9, 0x10000000
	v_cmp_le_u32_e32 vcc, s10, v0
	s_bcnt1_i32_b64 s88, vcc
	s_cmp_gt_u32 s88, 15
	s_cselect_b32 s9, s10, s9
	s_or_b32 s10, s9, 0x8000000
	v_cmp_le_u32_e32 vcc, s10, v0
	s_bcnt1_i32_b64 s88, vcc
	s_cmp_gt_u32 s88, 15
	s_cselect_b32 s9, s10, s9
	s_or_b32 s10, s9, 0x4000000
	v_cmp_le_u32_e32 vcc, s10, v0
	s_bcnt1_i32_b64 s88, vcc
	s_cmp_gt_u32 s88, 15
	s_cselect_b32 s9, s10, s9
	s_or_b32 s10, s9, 0x2000000
	v_cmp_le_u32_e32 vcc, s10, v0
	s_bcnt1_i32_b64 s88, vcc
	s_cmp_gt_u32 s88, 15
	s_cselect_b32 s9, s10, s9
	s_or_b32 s10, s9, 0x1000000
	v_cmp_le_u32_e32 vcc, s10, v0
	s_bcnt1_i32_b64 s88, vcc
	s_cmp_gt_u32 s88, 15
	s_cselect_b32 s9, s10, s9
	s_or_b32 s10, s9, 0x800000
	v_cmp_le_u32_e32 vcc, s10, v0
	s_bcnt1_i32_b64 s88, vcc
	s_cmp_gt_u32 s88, 15
	s_cselect_b32 s9, s10, s9
	s_or_b32 s10, s9, 0x400000
	v_cmp_le_u32_e32 vcc, s10, v0
	s_bcnt1_i32_b64 s88, vcc
	s_cmp_gt_u32 s88, 15
	s_cselect_b32 s9, s10, s9
	s_or_b32 s10, s9, 0x200000
	v_cmp_le_u32_e32 vcc, s10, v0
	s_bcnt1_i32_b64 s88, vcc
	s_cmp_gt_u32 s88, 15
	s_cselect_b32 s9, s10, s9
	s_or_b32 s10, s9, 0x100000
	v_cmp_le_u32_e32 vcc, s10, v0
	s_bcnt1_i32_b64 s88, vcc
	s_cmp_gt_u32 s88, 15
	s_cselect_b32 s9, s10, s9
	s_or_b32 s10, s9, 0x80000
	v_cmp_le_u32_e32 vcc, s10, v0
	s_bcnt1_i32_b64 s88, vcc
	s_cmp_gt_u32 s88, 15
	s_cselect_b32 s9, s10, s9
	s_or_b32 s10, s9, 0x40000
	v_cmp_le_u32_e32 vcc, s10, v0
	s_bcnt1_i32_b64 s88, vcc
	s_cmp_gt_u32 s88, 15
	s_cselect_b32 s9, s10, s9
	s_or_b32 s10, s9, 0x20000
	v_cmp_le_u32_e32 vcc, s10, v0
	s_bcnt1_i32_b64 s88, vcc
	s_cmp_gt_u32 s88, 15
	s_cselect_b32 s9, s10, s9
	s_or_b32 s10, s9, 0x10000
	v_cmp_le_u32_e32 vcc, s10, v0
	s_bcnt1_i32_b64 s88, vcc
	s_cmp_gt_u32 s88, 15
	s_cselect_b32 s9, s10, s9
	s_or_b32 s10, s9, 0x8000
	v_cmp_le_u32_e32 vcc, s10, v0
	s_bcnt1_i32_b64 s88, vcc
	s_cmp_gt_u32 s88, 15
	s_cselect_b32 s9, s10, s9
	s_or_b32 s10, s9, 0x4000
	v_cmp_le_u32_e32 vcc, s10, v0
	s_bcnt1_i32_b64 s88, vcc
	s_cmp_gt_u32 s88, 15
	s_cselect_b32 s9, s10, s9
	s_or_b32 s10, s9, 0x2000
	v_cmp_le_u32_e32 vcc, s10, v0
	s_bcnt1_i32_b64 s88, vcc
	s_cmp_gt_u32 s88, 15
	s_cselect_b32 s9, s10, s9
	s_or_b32 s10, s9, 0x1000
	v_cmp_le_u32_e32 vcc, s10, v0
	s_bcnt1_i32_b64 s88, vcc
	s_cmp_gt_u32 s88, 15
	s_cselect_b32 s9, s10, s9
	s_or_b32 s10, s9, 0x800
	v_cmp_le_u32_e32 vcc, s10, v0
	s_bcnt1_i32_b64 s88, vcc
	s_cmp_gt_u32 s88, 15
	s_cselect_b32 s9, s10, s9
	s_or_b32 s10, s9, 0x400
	v_cmp_le_u32_e32 vcc, s10, v0
	s_bcnt1_i32_b64 s88, vcc
	s_cmp_gt_u32 s88, 15
	s_cselect_b32 s9, s10, s9
	s_or_b32 s10, s9, 0x200
	v_cmp_le_u32_e32 vcc, s10, v0
	s_bcnt1_i32_b64 s88, vcc
	s_cmp_gt_u32 s88, 15
	s_cselect_b32 s9, s10, s9
	s_or_b32 s10, s9, 0x100
	v_cmp_le_u32_e32 vcc, s10, v0
	s_bcnt1_i32_b64 s88, vcc
	s_cmp_gt_u32 s88, 15
	s_cselect_b32 s9, s10, s9
	s_or_b32 s10, s9, 0x80
	v_cmp_le_u32_e32 vcc, s10, v0
	s_bcnt1_i32_b64 s88, vcc
	s_cmp_gt_u32 s88, 15
	s_cselect_b32 s9, s10, s9
	s_or_b32 s10, s9, 64
	v_cmp_le_u32_e32 vcc, s10, v0
	s_bcnt1_i32_b64 s88, vcc
	s_cmp_gt_u32 s88, 15
	s_cselect_b32 s9, s10, s9
	s_or_b32 s10, s9, 32
	v_cmp_le_u32_e32 vcc, s10, v0
	s_bcnt1_i32_b64 s88, vcc
	s_cmp_gt_u32 s88, 15
	s_cselect_b32 s9, s10, s9
	s_or_b32 s10, s9, 16
	v_cmp_le_u32_e32 vcc, s10, v0
	s_bcnt1_i32_b64 s88, vcc
	s_cmp_gt_u32 s88, 15
	s_cselect_b32 s9, s10, s9
	s_or_b32 s10, s9, 8
	v_cmp_le_u32_e32 vcc, s10, v0
	s_bcnt1_i32_b64 s88, vcc
	s_cmp_gt_u32 s88, 15
	s_cselect_b32 s9, s10, s9
	s_or_b32 s10, s9, 4
	v_cmp_le_u32_e32 vcc, s10, v0
	s_bcnt1_i32_b64 s88, vcc
	s_cmp_gt_u32 s88, 15
	s_cselect_b32 s9, s10, s9
	s_or_b32 s10, s9, 2
	v_cmp_le_u32_e32 vcc, s10, v0
	s_bcnt1_i32_b64 s88, vcc
	s_cmp_gt_u32 s88, 15
	s_cselect_b32 s9, s10, s9
	s_or_b32 s10, s9, 1
	v_cmp_le_u32_e32 vcc, s10, v0
	s_bcnt1_i32_b64 s88, vcc
	s_cmp_gt_u32 s88, 15
	s_cselect_b32 s9, s10, s9
	v_cmp_lt_u32_e64 s[0:1], s9, v0
	s_bcnt1_i32_b64 s88, s[0:1]
	v_cmp_gt_u64_e64 s[42:43], s[88:89], 15
	v_cmp_eq_u32_e64 s[12:13], s9, v0
	s_mov_b64 s[10:11], 0
	s_and_b64 vcc, exec, s[42:43]
	s_cbranch_vccnz .LBB0_507
	s_sub_i32 s9, 16, s88
	s_mov_b32 s16, 0
